# layer-0 split: projection GEMM on 160 workgroups (3 rounds), mixers on 128; workgroups 128-159 join the 96 converting workgroups after the projection (static share of the last 688 tile pairs)
# speedup vs baseline: 1.0204x; 1.0131x over previous
; #define LAS __attribute__((address_space(3)))
; __device__ __forceinline__ int opaque_tid() { int t = threadIdx.x; asm volatile("" : "+v"(t)); return t; }
; __device__ __forceinline__ void ph_weights(const Params& p, LAS unsigned char* lds, const int p0, const int p1, const int wi, const int wn) {
;     const int tid = opaque_tid();
;     LAS unsigned* l32 = (LAS unsigned*)lds;
;     LAS bf16_t* l16 = (LAS bf16_t*)lds;
;     TDesc dA0, dA1, dB0, dB1; f32x4 a0[8], a1[8], b0[8], b1[8];
;     ...
;     int pi = p0 + wi; bool hA, hB;
;     PW_LOAD(pi, dA0, dA1, a0, a1, hA);
;     PW_LOAD(pi + wn, dB0, dB1, b0, b1, hB);
.LBB0_779:
	v_readlane_b32 s0, v249, 28
	s_nop 3
	s_add_u32 s0, s0, 80
	s_movk_i32 s70, 96
	s_movk_i32 s71, 0x1830
	s_branch .Lcv_common
.Lcv_late:
	v_readlane_b32 s0, v249, 28
	s_nop 3
	s_add_u32 s0, s0, 6064
	s_movk_i32 s70, 32
	s_movk_i32 s71, 0x1ae0
.Lcv_common:
	s_lshl_b32 s72, s70, 1
	s_add_u32 s73, s72, s70
	v_writelane_b32 v255, s29, 61
	s_waitcnt lgkmcnt(0)
	v_and_b32_e32 v166, 31, v0
	v_lshrrev_b32_e32 v167, 5, v0
	v_lshlrev_b32_e32 v168, 1, v167
	v_lshlrev_b32_e32 v169, 4, v166
	v_lshlrev_b32_e32 v170, 3, v167
	v_lshrrev_b32_e32 v1, 2, v167
	v_lshlrev_b32_e32 v1, 4, v1
	v_xor_b32_e32 v1, v169, v1
	v_lshl_add_u32 v154, v167, 9, v1
	v_xor_b32_e32 v155, 64, v154
	v_xor_b32_e32 v156, 0x80, v154
	v_xor_b32_e32 v157, 0xc0, v154
	v_and_b32_e32 v171, 15, v0
	v_lshrrev_b32_e32 v175, 4, v0
	v_lshlrev_b32_e32 v1, 2, v171
	v_xor_b32_e32 v1, v175, v1
	v_lshlrev_b32_e32 v174, 11, v171
	v_lshl_add_u32 v162, v1, 2, v174
	v_xor_b32_e32 v163, 0x80, v162
	v_xor_b32_e32 v164, 0x100, v162
	v_xor_b32_e32 v165, 0x180, v162
	v_lshlrev_b32_e32 v176, 4, v171
	v_add_u32_e32 v158, 0x10000, v154
	v_add_u32_e32 v159, 0x10000, v155
	v_add_u32_e32 v160, 0x10000, v156
	v_add_u32_e32 v161, 0x10000, v157
	v_add_u32_e32 v130, 0x10000, v162
	v_add_u32_e32 v131, 0x10000, v163
	v_add_u32_e32 v132, 0x10000, v164
	v_add_u32_e32 v133, 0x10000, v165
	s_mov_b32 s9, 3
	s_cmp_ge_u32 s0, 0xd70
	s_cselect_b32 s77, 1, 0
	s_mul_i32 s83, s77, 0xd70
	s_sub_u32 s78, s0, s83
	v_readlane_b32 s20, v249, 37
	v_readlane_b32 s21, v249, 38
	s_mov_b32 s29, 0
	s_cmpk_lt_u32 s78, 0xf0
	s_cbranch_scc1 .Lcv_win_A1
	s_cmpk_lt_u32 s78, 0x170
	s_cbranch_scc1 .Lcv_wout_A1
	s_cmpk_lt_u32 s78, 0x970
	s_cbranch_scc1 .Lcv_gu_A1
	s_sub_u32 s78, s78, 0x970
	s_lshr_b32 s83, s78, 6
	s_bfe_u32 s93, s78, 0x30003
	s_and_b32 s94, s78, 7
	s_mul_i32 s98, s77, 0x8000000
	s_lshl_b32 s95, s83, 23
	s_add_u32 s98, s98, s95
	s_lshl_b32 s95, s93, 20
	s_add_u32 s98, s98, s95
	s_lshl_b32 s95, s94, 10
	s_add_u32 s98, s98, s95
	s_mul_i32 s99, s77, 0x4000000
	s_add_u32 s99, s99, 0x14400000
	s_lshl_b32 s95, s83, 22
	s_add_u32 s99, s99, s95
	s_lshl_b32 s95, s94, 19
	s_add_u32 s99, s99, s95
	s_lshl_b32 s95, s93, 8
	s_add_u32 s99, s99, s95
	v_readlane_b32 s12, v249, 4
	v_readlane_b32 s13, v249, 5
	s_movk_i32 s22, 0x2000
	s_movk_i32 s23, 0x800
	s_mov_b32 s28, 0x40000
	s_branch .Lcv_fin_A1

; __device__ __forceinline__ void ph_weights(const Params& p, LAS unsigned char* lds, const int p0, const int p1, const int wi, const int wn) {
;     ...
;     int pi = p0 + wi; bool hA, hB;
;     PW_LOAD(pi, dA0, dA1, a0, a1, hA);
;     PW_LOAD(pi + wn, dB0, dB1, b0, b1, hB);
.Lcv_fin_A1:
	s_nop 3
	s_add_u32 s12, s12, s98
	s_addc_u32 s13, s13, 0
	s_add_u32 s14, s26, s99
	s_addc_u32 s15, s27, 0
	v_mad_u32_u24 v177, v168, s22, v169
	s_mov_b64 s[88:89], s[12:13]
	s_add_u32 s90, s12, s22
	s_addc_u32 s91, s13, 0
	s_lshl_b32 s92, s22, 5
	global_load_dwordx2 v[138:139], v170, s[20:21]
	global_load_dwordx2 v[140:141], v170, s[20:21] offset:128
	global_load_dwordx2 v[142:143], v170, s[20:21] offset:256
	global_load_dwordx2 v[144:145], v170, s[20:21] offset:384
	global_load_dwordx4 v[2:5], v177, s[88:89] nt
	global_load_dwordx4 v[34:37], v177, s[88:89] offset:512 nt
	global_load_dwordx4 v[6:9], v177, s[90:91] nt
	global_load_dwordx4 v[38:41], v177, s[90:91] offset:512 nt
	s_add_u32 s88, s88, s92
	s_addc_u32 s89, s89, 0
	s_add_u32 s90, s90, s92
	s_addc_u32 s91, s91, 0
	global_load_dwordx4 v[10:13], v177, s[88:89] nt
	global_load_dwordx4 v[42:45], v177, s[88:89] offset:512 nt
	global_load_dwordx4 v[14:17], v177, s[90:91] nt
	global_load_dwordx4 v[46:49], v177, s[90:91] offset:512 nt
	s_add_u32 s88, s88, s92
	s_addc_u32 s89, s89, 0
	s_add_u32 s90, s90, s92
	s_addc_u32 s91, s91, 0
	global_load_dwordx4 v[18:21], v177, s[88:89] nt
	global_load_dwordx4 v[50:53], v177, s[88:89] offset:512 nt
	global_load_dwordx4 v[22:25], v177, s[90:91] nt
	global_load_dwordx4 v[54:57], v177, s[90:91] offset:512 nt
	s_add_u32 s88, s88, s92
	s_addc_u32 s89, s89, 0
	s_add_u32 s90, s90, s92
	s_addc_u32 s91, s91, 0
	global_load_dwordx4 v[26:29], v177, s[88:89] nt
	global_load_dwordx4 v[58:61], v177, s[88:89] offset:512 nt
	global_load_dwordx4 v[30:33], v177, s[90:91] nt
	global_load_dwordx4 v[62:65], v177, s[90:91] offset:512 nt
	global_load_dword v1, v170, s[20:21]
	global_load_dword v1, v170, s[20:21]
	global_load_dword v1, v170, s[20:21]
	global_load_dword v1, v170, s[20:21]
	global_load_dword v1, v170, s[20:21]
	global_load_dword v1, v170, s[20:21]
	global_load_dword v1, v170, s[20:21]
	global_load_dword v1, v170, s[20:21]
	s_add_u32 s86, s0, s70
	s_cmp_ge_u32 s86, 0xd70
	s_cselect_b32 s77, 1, 0
	s_mul_i32 s83, s77, 0xd70
	s_sub_u32 s78, s86, s83
	v_readlane_b32 s36, v249, 37
	v_readlane_b32 s37, v249, 38
	s_mov_b32 s60, 0
	s_cmpk_lt_u32 s78, 0xf0
	s_cbranch_scc1 .Lcv_win_B2
	s_cmpk_lt_u32 s78, 0x170
	s_cbranch_scc1 .Lcv_wout_B2
	s_cmpk_lt_u32 s78, 0x970
	s_cbranch_scc1 .Lcv_gu_B2
	s_sub_u32 s78, s78, 0x970
	s_lshr_b32 s83, s78, 6
	s_bfe_u32 s93, s78, 0x30003
	s_and_b32 s94, s78, 7
	s_mul_i32 s98, s77, 0x8000000
	s_lshl_b32 s95, s83, 23
	s_add_u32 s98, s98, s95
	s_lshl_b32 s95, s93, 20
	s_add_u32 s98, s98, s95
	s_lshl_b32 s95, s94, 10
	s_add_u32 s98, s98, s95
	s_mul_i32 s99, s77, 0x4000000
	s_add_u32 s99, s99, 0x14400000
	s_lshl_b32 s95, s83, 22
	s_add_u32 s99, s99, s95
	s_lshl_b32 s95, s94, 19
	s_add_u32 s99, s99, s95
	s_lshl_b32 s95, s93, 8
	s_add_u32 s99, s99, s95
	v_readlane_b32 s30, v249, 4
	v_readlane_b32 s31, v249, 5
	s_movk_i32 s56, 0x2000
	s_movk_i32 s57, 0x800
	s_mov_b32 s59, 0x40000
	s_branch .Lcv_fin_B2

; #define PW_SYNC do { asm volatile("s_waitcnt lgkmcnt(0)" ::: "memory"); __builtin_amdgcn_s_barrier(); asm volatile("" ::: "memory"); } while (0)
; __device__ __forceinline__ void ph_weights(const Params& p, LAS unsigned char* lds, const int p0, const int p1, const int wi, const int wn) {
;     ...
;     while (hA) {
;         { PW_TOLDS(dA0, a0, a1); PW_SYNC; const TDesc s0 = dA0, s1 = dA1; PW_LOAD(pi + 2 * wn, dA0, dA1, a0, a1, hA); PW_STORE(s0, s1); PW_SYNC; }
;         if (!hB) break;
;         { PW_TOLDS(dB0, b0, b1); PW_SYNC; const TDesc s0 = dB0, s1 = dB1; PW_LOAD(pi + 3 * wn, dB0, dB1, b0, b1, hB); PW_STORE(s0, s1); PW_SYNC; }
;         pi += 2 * wn;
.Lcv_loop:
	s_and_b32 s8, s9, 1
	s_cmp_eq_u32 s8, 0
	s_cbranch_scc1 .Lcv_done
	s_mov_b64 s[84:85], s[14:15]
	s_mov_b32 s69, s23
	s_mov_b32 s75, s28
	s_mov_b32 s87, s29
	s_add_u32 s86, s0, s72
	s_cmp_lt_u32 s86, s71
	s_cbranch_scc1 .Lcv_dec_A
	s_andn2_b32 s9, s9, 1
	s_branch .Lcv_ld_A

; #define PW_SYNC do { asm volatile("s_waitcnt lgkmcnt(0)" ::: "memory"); __builtin_amdgcn_s_barrier(); asm volatile("" ::: "memory"); } while (0)
; __device__ __forceinline__ void ph_weights(const Params& p, LAS unsigned char* lds, const int p0, const int p1, const int wi, const int wn) {
;     ...
;     int pi = p0 + wi; bool hA, hB;
;     PW_LOAD(pi, dA0, dA1, a0, a1, hA);
;     PW_LOAD(pi + wn, dB0, dB1, b0, b1, hB);
;     while (hA) {
;         { PW_TOLDS(dA0, a0, a1); PW_SYNC; const TDesc s0 = dA0, s1 = dA1; PW_LOAD(pi + 2 * wn, dA0, dA1, a0, a1, hA); PW_STORE(s0, s1); PW_SYNC; }
;         if (!hB) break;
;         { PW_TOLDS(dB0, b0, b1); PW_SYNC; const TDesc s0 = dB0, s1 = dB1; PW_LOAD(pi + 3 * wn, dB0, dB1, b0, b1, hB); PW_STORE(s0, s1); PW_SYNC; }
.Lcv_nosc1_At:
	v_cvt_pk_bf16_f32 v18, v18, v22
	v_cvt_pk_bf16_f32 v19, v19, v23
	v_cvt_pk_bf16_f32 v20, v20, v24
	v_cvt_pk_bf16_f32 v21, v21, v25
	v_cvt_pk_bf16_f32 v50, v50, v54
	v_cvt_pk_bf16_f32 v51, v51, v55
	v_cvt_pk_bf16_f32 v52, v52, v56
	v_cvt_pk_bf16_f32 v53, v53, v57
	ds_write_b128 v156, v[18:21] offset:16384
	ds_write_b128 v156, v[50:53] offset:49152
	v_cvt_pk_bf16_f32 v26, v26, v30
	v_cvt_pk_bf16_f32 v27, v27, v31
	v_cvt_pk_bf16_f32 v28, v28, v32
	v_cvt_pk_bf16_f32 v29, v29, v33
	v_cvt_pk_bf16_f32 v58, v58, v62
	v_cvt_pk_bf16_f32 v59, v59, v63
	v_cvt_pk_bf16_f32 v60, v60, v64
	v_cvt_pk_bf16_f32 v61, v61, v65
	ds_write_b128 v157, v[26:29] offset:24576
	ds_write_b128 v157, v[58:61] offset:57344
	v_mad_u32_u24 v177, v168, s22, v169
	s_mov_b64 s[88:89], s[12:13]
	s_add_u32 s90, s12, s22
	s_addc_u32 s91, s13, 0
	s_lshl_b32 s92, s22, 5
	global_load_dwordx2 v[138:139], v170, s[20:21]
	global_load_dwordx2 v[140:141], v170, s[20:21] offset:128
	global_load_dwordx2 v[142:143], v170, s[20:21] offset:256
	global_load_dwordx2 v[144:145], v170, s[20:21] offset:384
	global_load_dwordx4 v[2:5], v177, s[88:89] nt
	global_load_dwordx4 v[34:37], v177, s[88:89] offset:512 nt
	global_load_dwordx4 v[6:9], v177, s[90:91] nt
	global_load_dwordx4 v[38:41], v177, s[90:91] offset:512 nt
	s_add_u32 s88, s88, s92
	s_addc_u32 s89, s89, 0
	s_add_u32 s90, s90, s92
	s_addc_u32 s91, s91, 0
	global_load_dwordx4 v[10:13], v177, s[88:89] nt
	global_load_dwordx4 v[42:45], v177, s[88:89] offset:512 nt
	global_load_dwordx4 v[14:17], v177, s[90:91] nt
	global_load_dwordx4 v[46:49], v177, s[90:91] offset:512 nt
	s_add_u32 s88, s88, s92
	s_addc_u32 s89, s89, 0
	s_add_u32 s90, s90, s92
	s_addc_u32 s91, s91, 0
	global_load_dwordx4 v[18:21], v177, s[88:89] nt
	global_load_dwordx4 v[50:53], v177, s[88:89] offset:512 nt
	global_load_dwordx4 v[22:25], v177, s[90:91] nt
	global_load_dwordx4 v[54:57], v177, s[90:91] offset:512 nt
	s_add_u32 s88, s88, s92
	s_addc_u32 s89, s89, 0
	s_add_u32 s90, s90, s92
	s_addc_u32 s91, s91, 0
	global_load_dwordx4 v[26:29], v177, s[88:89] nt
	global_load_dwordx4 v[58:61], v177, s[88:89] offset:512 nt
	global_load_dwordx4 v[30:33], v177, s[90:91] nt
	global_load_dwordx4 v[62:65], v177, s[90:91] offset:512 nt
	s_waitcnt lgkmcnt(0)
	s_barrier
	v_mad_u32_u24 v178, v175, s69, v176
	s_mov_b64 s[88:89], s[84:85]
	s_add_u32 s90, s84, s75
	s_addc_u32 s91, s85, 0
	s_lshl_b32 s92, s69, 5
	ds_read_b32 v228, v162
	ds_read_b32 v229, v162 offset:512
	ds_read_b32 v230, v162 offset:1024
	ds_read_b32 v231, v162 offset:1536
	ds_read_b32 v232, v162 offset:32768
	ds_read_b32 v233, v162 offset:33280
	ds_read_b32 v234, v162 offset:33792
	ds_read_b32 v235, v162 offset:34304
	s_waitcnt lgkmcnt(0)
	ds_read_b32 v204, v163
	ds_read_b32 v205, v163 offset:512
	ds_read_b32 v206, v163 offset:1024
	ds_read_b32 v207, v163 offset:1536
	ds_read_b32 v208, v163 offset:32768
	ds_read_b32 v209, v163 offset:33280
	ds_read_b32 v210, v163 offset:33792
	ds_read_b32 v211, v163 offset:34304
	global_store_dwordx4 v178, v[228:231], s[88:89] nt
	global_store_dwordx4 v178, v[232:235], s[90:91] nt
	s_add_u32 s88, s88, s92
	s_addc_u32 s89, s89, 0
	s_add_u32 s90, s90, s92
	s_addc_u32 s91, s91, 0
	s_waitcnt lgkmcnt(0)
	ds_read_b32 v228, v164
	ds_read_b32 v229, v164 offset:512
	ds_read_b32 v230, v164 offset:1024
	ds_read_b32 v231, v164 offset:1536
	ds_read_b32 v232, v164 offset:32768
	ds_read_b32 v233, v164 offset:33280
	ds_read_b32 v234, v164 offset:33792
	ds_read_b32 v235, v164 offset:34304
	global_store_dwordx4 v178, v[204:207], s[88:89] nt
	global_store_dwordx4 v178, v[208:211], s[90:91] nt
	s_add_u32 s88, s88, s92
	s_addc_u32 s89, s89, 0
	s_add_u32 s90, s90, s92
	s_addc_u32 s91, s91, 0
	s_waitcnt lgkmcnt(0)
	ds_read_b32 v204, v165
	ds_read_b32 v205, v165 offset:512
	ds_read_b32 v206, v165 offset:1024
	ds_read_b32 v207, v165 offset:1536
	ds_read_b32 v208, v165 offset:32768
	ds_read_b32 v209, v165 offset:33280
	ds_read_b32 v210, v165 offset:33792
	ds_read_b32 v211, v165 offset:34304
	global_store_dwordx4 v178, v[228:231], s[88:89] nt
	global_store_dwordx4 v178, v[232:235], s[90:91] nt
	s_add_u32 s88, s88, s92
	s_addc_u32 s89, s89, 0
	s_add_u32 s90, s90, s92
	s_addc_u32 s91, s91, 0
	s_waitcnt lgkmcnt(0)
	global_store_dwordx4 v178, v[204:207], s[88:89] nt
	global_store_dwordx4 v178, v[208:211], s[90:91] nt
	s_and_b32 s8, s9, 2
	s_cmp_eq_u32 s8, 0
	s_cbranch_scc1 .Lcv_done
	s_mov_b64 s[84:85], s[32:33]
	s_mov_b32 s69, s57
	s_mov_b32 s75, s59
	s_mov_b32 s87, s60
	s_add_u32 s86, s0, s73
	s_cmp_lt_u32 s86, s71
	s_cbranch_scc1 .Lcv_dec_B
	s_andn2_b32 s9, s9, 2
	s_branch .Lcv_ld_B

; #define PW_SYNC do { asm volatile("s_waitcnt lgkmcnt(0)" ::: "memory"); __builtin_amdgcn_s_barrier(); asm volatile("" ::: "memory"); } while (0)
; __device__ __forceinline__ void ph_weights(const Params& p, LAS unsigned char* lds, const int p0, const int p1, const int wi, const int wn) {
;     ...
;     int pi = p0 + wi; bool hA, hB;
;     PW_LOAD(pi, dA0, dA1, a0, a1, hA);
;     PW_LOAD(pi + wn, dB0, dB1, b0, b1, hB);
;     while (hA) {
;         { PW_TOLDS(dA0, a0, a1); PW_SYNC; const TDesc s0 = dA0, s1 = dA1; PW_LOAD(pi + 2 * wn, dA0, dA1, a0, a1, hA); PW_STORE(s0, s1); PW_SYNC; }
;         if (!hB) break;
;         { PW_TOLDS(dB0, b0, b1); PW_SYNC; const TDesc s0 = dB0, s1 = dB1; PW_LOAD(pi + 3 * wn, dB0, dB1, b0, b1, hB); PW_STORE(s0, s1); PW_SYNC; }
;         pi += 2 * wn;
;     }
.Lcv_nosc1_Bt:
	v_cvt_pk_bf16_f32 v82, v82, v86
	v_cvt_pk_bf16_f32 v83, v83, v87
	v_cvt_pk_bf16_f32 v84, v84, v88
	v_cvt_pk_bf16_f32 v85, v85, v89
	v_cvt_pk_bf16_f32 v114, v114, v118
	v_cvt_pk_bf16_f32 v115, v115, v119
	v_cvt_pk_bf16_f32 v116, v116, v120
	v_cvt_pk_bf16_f32 v117, v117, v121
	ds_write_b128 v160, v[82:85] offset:16384
	ds_write_b128 v160, v[114:117] offset:49152
	v_cvt_pk_bf16_f32 v90, v90, v94
	v_cvt_pk_bf16_f32 v91, v91, v95
	v_cvt_pk_bf16_f32 v92, v92, v96
	v_cvt_pk_bf16_f32 v93, v93, v97
	v_cvt_pk_bf16_f32 v122, v122, v126
	v_cvt_pk_bf16_f32 v123, v123, v127
	v_cvt_pk_bf16_f32 v124, v124, v128
	v_cvt_pk_bf16_f32 v125, v125, v129
	ds_write_b128 v161, v[90:93] offset:24576
	ds_write_b128 v161, v[122:125] offset:57344
	v_mad_u32_u24 v177, v168, s56, v169
	s_mov_b64 s[88:89], s[30:31]
	s_add_u32 s90, s30, s56
	s_addc_u32 s91, s31, 0
	s_lshl_b32 s92, s56, 5
	global_load_dwordx2 v[146:147], v170, s[36:37]
	global_load_dwordx2 v[148:149], v170, s[36:37] offset:128
	global_load_dwordx2 v[150:151], v170, s[36:37] offset:256
	global_load_dwordx2 v[152:153], v170, s[36:37] offset:384
	global_load_dwordx4 v[66:69], v177, s[88:89] nt
	global_load_dwordx4 v[98:101], v177, s[88:89] offset:512 nt
	global_load_dwordx4 v[70:73], v177, s[90:91] nt
	global_load_dwordx4 v[102:105], v177, s[90:91] offset:512 nt
	s_add_u32 s88, s88, s92
	s_addc_u32 s89, s89, 0
	s_add_u32 s90, s90, s92
	s_addc_u32 s91, s91, 0
	global_load_dwordx4 v[74:77], v177, s[88:89] nt
	global_load_dwordx4 v[106:109], v177, s[88:89] offset:512 nt
	global_load_dwordx4 v[78:81], v177, s[90:91] nt
	global_load_dwordx4 v[110:113], v177, s[90:91] offset:512 nt
	s_add_u32 s88, s88, s92
	s_addc_u32 s89, s89, 0
	s_add_u32 s90, s90, s92
	s_addc_u32 s91, s91, 0
	global_load_dwordx4 v[82:85], v177, s[88:89] nt
	global_load_dwordx4 v[114:117], v177, s[88:89] offset:512 nt
	global_load_dwordx4 v[86:89], v177, s[90:91] nt
	global_load_dwordx4 v[118:121], v177, s[90:91] offset:512 nt
	s_add_u32 s88, s88, s92
	s_addc_u32 s89, s89, 0
	s_add_u32 s90, s90, s92
	s_addc_u32 s91, s91, 0
	global_load_dwordx4 v[90:93], v177, s[88:89] nt
	global_load_dwordx4 v[122:125], v177, s[88:89] offset:512 nt
	global_load_dwordx4 v[94:97], v177, s[90:91] nt
	global_load_dwordx4 v[126:129], v177, s[90:91] offset:512 nt
	s_waitcnt lgkmcnt(0)
	s_barrier
	v_mad_u32_u24 v178, v175, s69, v176
	s_mov_b64 s[88:89], s[84:85]
	s_add_u32 s90, s84, s75
	s_addc_u32 s91, s85, 0
	s_lshl_b32 s92, s69, 5
	ds_read_b32 v228, v130
	ds_read_b32 v229, v130 offset:512
	ds_read_b32 v230, v130 offset:1024
	ds_read_b32 v231, v130 offset:1536
	ds_read_b32 v232, v130 offset:32768
	ds_read_b32 v233, v130 offset:33280
	ds_read_b32 v234, v130 offset:33792
	ds_read_b32 v235, v130 offset:34304
	s_waitcnt lgkmcnt(0)
	ds_read_b32 v204, v131
	ds_read_b32 v205, v131 offset:512
	ds_read_b32 v206, v131 offset:1024
	ds_read_b32 v207, v131 offset:1536
	ds_read_b32 v208, v131 offset:32768
	ds_read_b32 v209, v131 offset:33280
	ds_read_b32 v210, v131 offset:33792
	ds_read_b32 v211, v131 offset:34304
	global_store_dwordx4 v178, v[228:231], s[88:89] nt
	global_store_dwordx4 v178, v[232:235], s[90:91] nt
	s_add_u32 s88, s88, s92
	s_addc_u32 s89, s89, 0
	s_add_u32 s90, s90, s92
	s_addc_u32 s91, s91, 0
	s_waitcnt lgkmcnt(0)
	ds_read_b32 v228, v132
	ds_read_b32 v229, v132 offset:512
	ds_read_b32 v230, v132 offset:1024
	ds_read_b32 v231, v132 offset:1536
	ds_read_b32 v232, v132 offset:32768
	ds_read_b32 v233, v132 offset:33280
	ds_read_b32 v234, v132 offset:33792
	ds_read_b32 v235, v132 offset:34304
	global_store_dwordx4 v178, v[204:207], s[88:89] nt
	global_store_dwordx4 v178, v[208:211], s[90:91] nt
	s_add_u32 s88, s88, s92
	s_addc_u32 s89, s89, 0
	s_add_u32 s90, s90, s92
	s_addc_u32 s91, s91, 0
	s_waitcnt lgkmcnt(0)
	ds_read_b32 v204, v133
	ds_read_b32 v205, v133 offset:512
	ds_read_b32 v206, v133 offset:1024
	ds_read_b32 v207, v133 offset:1536
	ds_read_b32 v208, v133 offset:32768
	ds_read_b32 v209, v133 offset:33280
	ds_read_b32 v210, v133 offset:33792
	ds_read_b32 v211, v133 offset:34304
	global_store_dwordx4 v178, v[228:231], s[88:89] nt
	global_store_dwordx4 v178, v[232:235], s[90:91] nt
	s_add_u32 s88, s88, s92
	s_addc_u32 s89, s89, 0
	s_add_u32 s90, s90, s92
	s_addc_u32 s91, s91, 0
	s_waitcnt lgkmcnt(0)
	global_store_dwordx4 v178, v[204:207], s[88:89] nt
	global_store_dwordx4 v178, v[208:211], s[90:91] nt
	s_add_u32 s0, s0, s72
	s_branch .Lcv_loop

; #define REP(k) _Pragma("unroll") for (int rep_ = 0; rep_ < 1 + (int)(((REP_MASK) >> (k)) & 1u); ++rep_)
; #define SEAM(k) do { if (IN(k) && IN((k) + 1)) xcd_barrier(bar); } while (0)
; __global__ void __launch_bounds__(512, 2) mk_fwd(Params p) {
;     ...
;         if (split) { if (bx < MIX_GW && IN(pb + 1) && IN(pb + 2)) xcd_barrier(bar2); } else SEAM(pb + 1);
;         if (IN(pb + 2)) {
;             if (!split || bx < MIX_GW) {
;                 if (EN(5)) REP(5) ph_fft(p, lds, bx, vG);
;                 __syncthreads();
;                 if (EN(8)) REP(8) ph_mixers(p, l, lds, bx, vG);
;             } else { if (bx - MIX_GW < 4) ph_rbias(p, 0, bx - MIX_GW); ph_weights(p, lds, 240, 6880, bx - MIX_GW, G - MIX_GW); }
.Lcv_mixdisp:
	v_readlane_b32 s8, v252, 58
	v_readlane_b32 s9, v252, 59
	s_nop 3
	s_and_b64 s[8:9], s[8:9], exec
	s_cbranch_scc0 .LBB0_903
	s_movk_i32 s29, 0x80
	v_readlane_b32 s8, v249, 28
	s_nop 3
	s_cmpk_lt_u32 s8, 0x80
	s_cbranch_scc1 .LBB0_903
	s_branch .Lcv_late
